# grid barrier: non-leader workgroups wait on the cross-XCD release word directly (on top of v21)
# speedup vs baseline: 1.0071x; 1.0005x over previous
.LBB0_58:
	s_or_b64 exec, exec, s[12:13]
	v_cvt_f32_u32_e32 v5, v3
	s_waitcnt vmcnt(0)
	v_readfirstlane_b32 s3, v4
	v_sub_u32_e32 v4, 0, v3
	v_rcp_iflag_f32_e32 v5, v5
	v_add_u32_e32 v6, s3, v2
	v_mul_f32_e32 v5, 0x4f7ffffe, v5
	v_cvt_u32_f32_e32 v5, v5
	v_mul_lo_u32 v2, v4, v5
	v_mul_hi_u32 v2, v5, v2
	v_add_u32_e32 v2, v5, v2
	v_mul_hi_u32 v2, v6, v2
	v_mul_lo_u32 v4, v2, v3
	v_sub_u32_e32 v4, v6, v4
	v_add_u32_e32 v5, 1, v2
	v_cmp_ge_u32_e32 vcc, v4, v3
	s_nop 1
	v_cndmask_b32_e32 v2, v2, v5, vcc
	v_sub_u32_e32 v5, v4, v3
	v_cndmask_b32_e32 v4, v4, v5, vcc
	v_add_u32_e32 v5, 1, v2
	v_cmp_ge_u32_e32 vcc, v4, v3
	v_add_u32_e32 v4, 1, v6
	s_nop 0
	v_cndmask_b32_e32 v2, v2, v5, vcc
	v_mul_lo_u32 v5, v3, v2
	v_add_u32_e32 v3, v5, v3
	v_cmp_ne_u32_e32 vcc, v4, v3
	s_and_saveexec_b64 s[10:11], vcc
	s_xor_b64 s[10:11], exec, s[10:11]
	s_cbranch_execz .LBB0_72
	s_waitcnt lgkmcnt(0)
	v_mov_b32_e32 v1, 0x3500
	global_load_dword v1, v1, s[44:45] sc1
	buffer_inv sc1
	s_add_u32 s14, s44, 0x3500
	s_addc_u32 s15, s45, 0
	s_waitcnt vmcnt(0)
	v_cmp_eq_u32_e32 vcc, v1, v2
	s_and_saveexec_b64 s[12:13], vcc
	s_cbranch_execz .LBB0_71
	s_mov_b32 s3, 1
	s_mov_b64 s[16:17], 0
	v_mov_b32_e32 v1, 0
	s_branch .LBB0_62

.LBB0_256:
	s_or_b64 exec, exec, s[12:13]
	v_cvt_f32_u32_e32 v6, v4
	s_waitcnt vmcnt(0)
	v_readfirstlane_b32 s3, v5
	v_sub_u32_e32 v5, 0, v4
	v_rcp_iflag_f32_e32 v6, v6
	v_add_u32_e32 v7, s3, v3
	v_mul_f32_e32 v6, 0x4f7ffffe, v6
	v_cvt_u32_f32_e32 v6, v6
	v_mul_lo_u32 v3, v5, v6
	v_mul_hi_u32 v3, v6, v3
	v_add_u32_e32 v3, v6, v3
	v_mul_hi_u32 v3, v7, v3
	v_mul_lo_u32 v5, v3, v4
	v_sub_u32_e32 v5, v7, v5
	v_add_u32_e32 v6, 1, v3
	v_cmp_ge_u32_e32 vcc, v5, v4
	s_nop 1
	v_cndmask_b32_e32 v3, v3, v6, vcc
	v_sub_u32_e32 v6, v5, v4
	v_cndmask_b32_e32 v5, v5, v6, vcc
	v_add_u32_e32 v6, 1, v3
	v_cmp_ge_u32_e32 vcc, v5, v4
	v_add_u32_e32 v5, 1, v7
	s_nop 0
	v_cndmask_b32_e32 v3, v3, v6, vcc
	v_mul_lo_u32 v6, v4, v3
	v_add_u32_e32 v4, v6, v4
	v_cmp_ne_u32_e32 vcc, v5, v4
	s_and_saveexec_b64 s[10:11], vcc
	s_xor_b64 s[10:11], exec, s[10:11]
	s_cbranch_execz .LBB0_270
	s_waitcnt lgkmcnt(0)
	v_mov_b32_e32 v2, 0x3500
	global_load_dword v2, v2, s[44:45] sc1
	buffer_inv sc1
	s_add_u32 s14, s44, 0x3500
	s_addc_u32 s15, s45, 0
	s_waitcnt vmcnt(0)
	v_cmp_eq_u32_e32 vcc, v2, v3
	s_and_saveexec_b64 s[12:13], vcc
	s_cbranch_execz .LBB0_269
	s_mov_b32 s3, 1
	s_mov_b64 s[16:17], 0
	v_mov_b32_e32 v2, 0
	s_branch .LBB0_260

.LBB0_1490:
	s_or_b64 exec, exec, s[14:15]
	v_cvt_f32_u32_e32 v6, v4
	s_waitcnt vmcnt(0)
	v_readfirstlane_b32 s3, v5
	v_sub_u32_e32 v5, 0, v4
	v_rcp_iflag_f32_e32 v6, v6
	v_add_u32_e32 v7, s3, v3
	v_mul_f32_e32 v6, 0x4f7ffffe, v6
	v_cvt_u32_f32_e32 v6, v6
	v_mul_lo_u32 v3, v5, v6
	v_mul_hi_u32 v3, v6, v3
	v_add_u32_e32 v3, v6, v3
	v_mul_hi_u32 v3, v7, v3
	v_mul_lo_u32 v5, v3, v4
	v_sub_u32_e32 v5, v7, v5
	v_add_u32_e32 v6, 1, v3
	v_cmp_ge_u32_e32 vcc, v5, v4
	s_nop 1
	v_cndmask_b32_e32 v3, v3, v6, vcc
	v_sub_u32_e32 v6, v5, v4
	v_cndmask_b32_e32 v5, v5, v6, vcc
	v_add_u32_e32 v6, 1, v3
	v_cmp_ge_u32_e32 vcc, v5, v4
	v_add_u32_e32 v5, 1, v7
	s_nop 0
	v_cndmask_b32_e32 v3, v3, v6, vcc
	v_mul_lo_u32 v6, v4, v3
	v_add_u32_e32 v4, v6, v4
	v_cmp_ne_u32_e32 vcc, v5, v4
	s_and_saveexec_b64 s[12:13], vcc
	s_xor_b64 s[12:13], exec, s[12:13]
	s_cbranch_execz .LBB0_1504
	s_waitcnt lgkmcnt(0)
	v_mov_b32_e32 v2, 0x3500
	global_load_dword v2, v2, s[44:45] sc1
	buffer_inv sc1
	s_add_u32 s16, s44, 0x3500
	s_addc_u32 s17, s45, 0
	s_waitcnt vmcnt(0)
	v_cmp_eq_u32_e32 vcc, v2, v3
	s_and_saveexec_b64 s[14:15], vcc
	s_cbranch_execz .LBB0_1503
	s_mov_b32 s3, 1
	s_mov_b64 s[18:19], 0
	v_mov_b32_e32 v2, 0
	s_branch .LBB0_1494

.LBB0_1954:
	s_or_b64 exec, exec, s[12:13]
	v_cvt_f32_u32_e32 v6, v4
	s_waitcnt vmcnt(0)
	v_readfirstlane_b32 s10, v5
	v_sub_u32_e32 v5, 0, v4
	v_rcp_iflag_f32_e32 v6, v6
	v_add_u32_e32 v7, s10, v3
	v_mul_f32_e32 v6, 0x4f7ffffe, v6
	v_cvt_u32_f32_e32 v6, v6
	v_mul_lo_u32 v3, v5, v6
	v_mul_hi_u32 v3, v6, v3
	v_add_u32_e32 v3, v6, v3
	v_mul_hi_u32 v3, v7, v3
	v_mul_lo_u32 v5, v3, v4
	v_sub_u32_e32 v5, v7, v5
	v_add_u32_e32 v6, 1, v3
	v_cmp_ge_u32_e32 vcc, v5, v4
	s_nop 1
	v_cndmask_b32_e32 v3, v3, v6, vcc
	v_sub_u32_e32 v6, v5, v4
	v_cndmask_b32_e32 v5, v5, v6, vcc
	v_add_u32_e32 v6, 1, v3
	v_cmp_ge_u32_e32 vcc, v5, v4
	v_add_u32_e32 v5, 1, v7
	s_nop 0
	v_cndmask_b32_e32 v3, v3, v6, vcc
	v_mul_lo_u32 v6, v4, v3
	v_add_u32_e32 v4, v6, v4
	v_cmp_ne_u32_e32 vcc, v5, v4
	s_and_saveexec_b64 s[10:11], vcc
	s_xor_b64 s[10:11], exec, s[10:11]
	s_cbranch_execz .LBB0_1968
	s_waitcnt lgkmcnt(0)
	v_mov_b32_e32 v2, 0x3500
	global_load_dword v2, v2, s[44:45] sc1
	buffer_inv sc1
	s_add_u32 s14, s44, 0x3500
	s_addc_u32 s15, s45, 0
	s_waitcnt vmcnt(0)
	v_cmp_eq_u32_e32 vcc, v2, v3
	s_and_saveexec_b64 s[12:13], vcc
	s_cbranch_execz .LBB0_1967
	s_mov_b32 s26, 1
	s_mov_b64 s[16:17], 0
	v_mov_b32_e32 v2, 0
	s_branch .LBB0_1958

.LBB0_2010:
	s_or_b64 exec, exec, s[10:11]
	v_cvt_f32_u32_e32 v6, v4
	s_waitcnt vmcnt(0)
	v_readfirstlane_b32 s8, v5
	v_sub_u32_e32 v5, 0, v4
	v_rcp_iflag_f32_e32 v6, v6
	v_add_u32_e32 v7, s8, v3
	v_mul_f32_e32 v6, 0x4f7ffffe, v6
	v_cvt_u32_f32_e32 v6, v6
	v_mul_lo_u32 v3, v5, v6
	v_mul_hi_u32 v3, v6, v3
	v_add_u32_e32 v3, v6, v3
	v_mul_hi_u32 v3, v7, v3
	v_mul_lo_u32 v5, v3, v4
	v_sub_u32_e32 v5, v7, v5
	v_add_u32_e32 v6, 1, v3
	v_cmp_ge_u32_e32 vcc, v5, v4
	s_nop 1
	v_cndmask_b32_e32 v3, v3, v6, vcc
	v_sub_u32_e32 v6, v5, v4
	v_cndmask_b32_e32 v5, v5, v6, vcc
	v_add_u32_e32 v6, 1, v3
	v_cmp_ge_u32_e32 vcc, v5, v4
	v_add_u32_e32 v5, 1, v7
	s_nop 0
	v_cndmask_b32_e32 v3, v3, v6, vcc
	v_mul_lo_u32 v6, v4, v3
	v_add_u32_e32 v4, v6, v4
	v_cmp_ne_u32_e32 vcc, v5, v4
	s_and_saveexec_b64 s[8:9], vcc
	s_xor_b64 s[8:9], exec, s[8:9]
	s_cbranch_execz .LBB0_2024
	s_waitcnt lgkmcnt(0)
	v_mov_b32_e32 v2, 0x3500
	global_load_dword v2, v2, s[44:45] sc1
	buffer_inv sc1
	s_add_u32 s12, s44, 0x3500
	s_addc_u32 s13, s45, 0
	s_waitcnt vmcnt(0)
	v_cmp_eq_u32_e32 vcc, v2, v3
	s_and_saveexec_b64 s[10:11], vcc
	s_cbranch_execz .LBB0_2023
	s_mov_b32 s24, 1
	s_mov_b64 s[14:15], 0
	v_mov_b32_e32 v2, 0
	s_branch .LBB0_2014

.LBB0_2102:
	s_or_b64 exec, exec, s[8:9]
	v_cvt_f32_u32_e32 v5, v3
	s_waitcnt vmcnt(0)
	v_readfirstlane_b32 s6, v4
	v_sub_u32_e32 v4, 0, v3
	v_rcp_iflag_f32_e32 v5, v5
	v_add_u32_e32 v6, s6, v2
	v_mul_f32_e32 v5, 0x4f7ffffe, v5
	v_cvt_u32_f32_e32 v5, v5
	v_mul_lo_u32 v2, v4, v5
	v_mul_hi_u32 v2, v5, v2
	v_add_u32_e32 v2, v5, v2
	v_mul_hi_u32 v2, v6, v2
	v_mul_lo_u32 v4, v2, v3
	v_sub_u32_e32 v4, v6, v4
	v_add_u32_e32 v5, 1, v2
	v_cmp_ge_u32_e32 vcc, v4, v3
	s_nop 1
	v_cndmask_b32_e32 v2, v2, v5, vcc
	v_sub_u32_e32 v5, v4, v3
	v_cndmask_b32_e32 v4, v4, v5, vcc
	v_add_u32_e32 v5, 1, v2
	v_cmp_ge_u32_e32 vcc, v4, v3
	v_add_u32_e32 v4, 1, v6
	s_nop 0
	v_cndmask_b32_e32 v2, v2, v5, vcc
	v_mul_lo_u32 v5, v3, v2
	v_add_u32_e32 v3, v5, v3
	v_cmp_ne_u32_e32 vcc, v4, v3
	s_and_saveexec_b64 s[6:7], vcc
	s_xor_b64 s[6:7], exec, s[6:7]
	s_cbranch_execz .LBB0_2116
	s_waitcnt lgkmcnt(0)
	v_mov_b32_e32 v1, 0x3500
	global_load_dword v1, v1, s[44:45] sc1
	buffer_inv sc1
	s_add_u32 s10, s44, 0x3500
	s_addc_u32 s11, s45, 0
	s_waitcnt vmcnt(0)
	v_cmp_eq_u32_e32 vcc, v1, v2
	s_and_saveexec_b64 s[8:9], vcc
	s_cbranch_execz .LBB0_2115
	s_mov_b32 s22, 1
	s_mov_b64 s[12:13], 0
	v_mov_b32_e32 v1, 0
	s_branch .LBB0_2106
